# n8_opt_early_ack
# speedup vs baseline: 1.0185x; 1.0185x over previous
.LBB2_15:
	v_ashrrev_i32_e32 v163, 31, v162
	v_lshl_or_b32 v164, s30, 4, v132
	v_lshlrev_b64 v[130:131], 11, v[162:163]
	v_mov_b32_e32 v167, 0
	s_waitcnt lgkmcnt(0)
	s_mov_b64 s[50:51], s[0:1]
	v_lshl_add_u64 v[130:131], s[0:1], 0, v[130:131]
	v_lshlrev_b32_e32 v166, 4, v164
	v_lshl_add_u64 v[168:169], v[130:131], 0, v[166:167]
	global_load_dwordx2 v[170:171], v[168:169], off nt
	v_lshlrev_b32_e32 v142, 4, v140
	v_cmp_gt_u32_e64 s[2:3], 16, v140
	v_mov_b32_e32 v140, 0x10000
	v_lshlrev_b32_e32 v130, 8, v139
	v_lshlrev_b32_e32 v131, 4, v132
	v_lshlrev_b32_e32 v132, 3, v138
	v_lshl_or_b32 v177, v138, 14, v142
	v_lshl_or_b32 v139, v139, 11, v140
	v_lshlrev_b32_e32 v140, 10, v138
	v_xor_b32_e32 v138, 1, v138
	v_lshlrev_b32_e32 v141, 12, v1
	v_lshlrev_b32_e32 v138, 10, v138
	v_or3_b32 v179, v139, v138, v142
	v_add_u32_e32 v138, 0x1000, v141
	v_and_b32_e32 v180, 0x3000, v138
	v_add_u32_e32 v138, 0x1400, v141
	v_and_b32_e32 v181, 0x3400, v138
	v_add_u32_e32 v138, 0x1800, v141
	v_and_b32_e32 v182, 0x3800, v138
	v_add_u32_e32 v138, 0x1c00, v141
	v_and_b32_e32 v183, 0x3c00, v138
	s_movk_i32 s4, 0x2000
	v_mov_b32_e32 v138, 0x3000
	v_bitop3_b32 v184, v141, s4, v138 bitop3:0x6c
	v_add_u32_e32 v138, 0x2400, v141
	v_and_b32_e32 v185, 0x3400, v138
	v_add_u32_e32 v138, 0x2800, v141
	v_and_b32_e32 v186, 0x3800, v138
	v_add_u32_e32 v138, 0x2c00, v141
	v_and_b32_e32 v187, 0x3c00, v138
	v_add_u32_e32 v138, 0x3000, v141
	v_and_b32_e32 v188, 0x3000, v138
	v_add_u32_e32 v138, 0x3400, v141
	s_and_b32 s9, s7, 0xffff
	v_cmp_eq_u32_e32 vcc, s14, v133
	v_lshl_or_b32 v131, s16, 10, v131
	s_movk_i32 s0, 0x100
	v_lshlrev_b32_e32 v166, 12, v164
	v_and_b32_e32 v189, 0x3400, v138
	v_add_u32_e32 v138, 0x3800, v141
	s_cmp_lg_u64 vcc, exec
	v_lshl_add_u32 v131, s30, 15, v131
	v_cmp_gt_u32_e64 s[0:1], s0, v0
	v_lshl_add_u64 v[0:1], s[12:13], 0, v[166:167]
	v_and_b32_e32 v190, 0x3800, v138
	v_add_u32_e32 v138, 0x3c00, v141
	v_mov_b32_e32 v172, -1
	s_mov_b32 s11, 0x20000
	s_mov_b32 s10, 0x200400
	s_mov_b32 s8, s6
	s_cselect_b64 s[14:15], -1, 0
	v_or3_b32 v165, v131, v132, v130
	s_mov_b32 s17, 0
	v_cndmask_b32_e64 v133, 0, v137, s[0:1]
	v_cndmask_b32_e64 v132, 0, v136, s[0:1]
	v_cndmask_b32_e64 v131, 0, v135, s[0:1]
	v_cndmask_b32_e64 v130, 0, v134, s[0:1]
	v_cndmask_b32_e64 v137, v137, 0, s[0:1]
	v_cndmask_b32_e64 v136, v136, 0, s[0:1]
	v_cndmask_b32_e64 v135, v135, 0, s[0:1]
	v_cndmask_b32_e64 v134, v134, 0, s[0:1]
	v_or_b32_e32 v176, v141, v142
	v_lshl_add_u64 v[0:1], v[162:163], 2, v[0:1]
	v_or3_b32 v178, v139, v140, v142
	v_and_b32_e32 v191, 0x3c00, v138
	s_mov_b64 s[24:25], 0
	s_mov_b64 s[18:19], 0x400
	s_mov_b64 s[20:21], 0x800
	s_mov_b64 s[22:23], 0xc00
	s_mov_b32 s31, 0x40004000
	v_mov_b32_e32 v173, v172
	v_mov_b32_e32 v192, 0
	v_mov_b32_e32 v193, 0
	s_mov_b32 s33, 0
	v_add_u32_e32 v180, v180, v177
	v_add_u32_e32 v181, v181, v177
	v_add_u32_e32 v182, v182, v177
	v_add_u32_e32 v183, v183, v177
	v_add_u32_e32 v184, v184, v177
	v_add_u32_e32 v185, v185, v177
	v_add_u32_e32 v186, v186, v177
	v_add_u32_e32 v187, v187, v177
	v_add_u32_e32 v188, v188, v177
	v_add_u32_e32 v189, v189, v177
	v_add_u32_e32 v190, v190, v177
	v_add_u32_e32 v191, v191, v177
	v_mov_b32_e32 v166, v176
	v_lshlrev_b32_e32 v242, 12, v164
	v_lshl_add_u32 v242, v162, 2, v242
	v_lshlrev_b32_e32 v243, 11, v162
	v_lshl_add_u32 v243, v164, 4, v243
	v_readfirstlane_b32 s42, v176
	s_or_b32 s42, s42, 0x8000
	s_mov_b32 m0, s42
	s_lshl_b32 s36, s30, 15
	s_add_u32 s54, s6, s36
	s_addc_u32 s55, s7, 0
	s_mov_b64 s[40:41], s[54:55]
	s_mov_b32 s45, 0
	s_mov_b32 s58, 0x40000
	s_mov_b32 s46, 0x180000
	s_mov_b64 s[48:49], s[12:13]
	s_cmp_lg_u64 s[14:15], 0
	s_cselect_b32 s57, 1, 0
	s_cmp_lg_u64 s[0:1], 0
	s_cselect_b32 s59, 1, 0
	s_mov_b32 s47, 0
	s_add_u32 s52, s50, 8
	s_addc_u32 s53, s51, 0
	global_load_dwordx2 v[174:175], v243, s[52:53] nt
	s_add_u32 s52, s50, 0x200000
	s_addc_u32 s53, s51, 0
	s_waitcnt vmcnt(1)
	v_cvt_f32_f16_e32 v250, v170
	v_cvt_f32_f16_sdwa v251, v170 dst_sel:DWORD dst_unused:UNUSED_PAD src0_sel:WORD_1
	v_cvt_f32_f16_e32 v252, v171
	v_cvt_f32_f16_sdwa v253, v171 dst_sel:DWORD dst_unused:UNUSED_PAD src0_sel:WORD_1
	v_pk_add_f32 v[198:199], v[130:131], v[134:135]
	v_pk_add_f32 v[200:201], v[132:133], v[136:137]
	v_mov_b32_e32 v194, 0
	v_mov_b32_e32 v195, 0
	v_mov_b32_e32 v196, 0
	v_mov_b32_e32 v197, 0
	v_pk_add_f32 v[198:199], v[198:199], v[250:251]
	v_pk_add_f32 v[200:201], v[200:201], v[252:253]
	s_branch .Lrec_act
.Lrec_step:
	global_load_lds_dwordx4 v176, s[40:41] sc1
	global_load_lds_dwordx4 v176, s[40:41] offset:1024 sc1
	global_load_lds_dwordx4 v176, s[40:41] offset:2048 sc1
	global_load_lds_dwordx4 v176, s[40:41] offset:3072 sc1
	s_mov_b32 s45, s58
	s_mov_b32 s44, 0
	v_xor_b32_e32 v166, 0x8000, v166
	v_xor_b32_e32 v180, 0x8000, v180
	v_xor_b32_e32 v181, 0x8000, v181
	v_xor_b32_e32 v182, 0x8000, v182
	v_xor_b32_e32 v183, 0x8000, v183
	v_xor_b32_e32 v184, 0x8000, v184
	v_xor_b32_e32 v185, 0x8000, v185
	v_xor_b32_e32 v186, 0x8000, v186
	v_xor_b32_e32 v187, 0x8000, v187
	v_xor_b32_e32 v188, 0x8000, v188
	v_xor_b32_e32 v189, 0x8000, v189
	v_xor_b32_e32 v190, 0x8000, v190
	v_xor_b32_e32 v191, 0x8000, v191
	s_waitcnt vmcnt(4)
	v_cvt_f32_f16_e32 v250, v174
	v_cvt_f32_f16_sdwa v251, v174 dst_sel:DWORD dst_unused:UNUSED_PAD src0_sel:WORD_1
	v_cvt_f32_f16_e32 v252, v175
	v_cvt_f32_f16_sdwa v253, v175 dst_sel:DWORD dst_unused:UNUSED_PAD src0_sel:WORD_1
.Lrec_own:
	s_waitcnt vmcnt(3)
	ds_read_b128 v[138:141], v166
	s_waitcnt vmcnt(2)
	ds_read_b128 v[142:145], v166 offset:1024
	s_waitcnt vmcnt(1)
	ds_read_b128 v[146:149], v166 offset:2048
	s_waitcnt vmcnt(0)
	ds_read_b128 v[150:153], v166 offset:3072
	s_waitcnt lgkmcnt(3)
	v_mfma_f32_16x16x32_f16 v[158:161], v[2:5], v[138:141], v[130:133]
	v_mfma_f32_16x16x32_f16 v[154:157], v[66:69], v[138:141], v[134:137]
	s_waitcnt lgkmcnt(2)
	v_mfma_f32_16x16x32_f16 v[158:161], v[6:9], v[142:145], v[158:161]
	v_mfma_f32_16x16x32_f16 v[154:157], v[70:73], v[142:145], v[154:157]
	s_waitcnt lgkmcnt(1)
	v_mfma_f32_16x16x32_f16 v[158:161], v[10:13], v[146:149], v[158:161]
	v_mfma_f32_16x16x32_f16 v[154:157], v[74:77], v[146:149], v[154:157]
	s_waitcnt lgkmcnt(0)
	v_mfma_f32_16x16x32_f16 v[158:161], v[14:17], v[150:153], v[158:161]
	v_mfma_f32_16x16x32_f16 v[154:157], v[78:81], v[150:153], v[154:157]
	v_or3_b32 v249, v138, v139, v140
	v_or3_b32 v249, v249, v141, v142
	v_or3_b32 v249, v249, v143, v144
	v_or3_b32 v249, v249, v145, v146
	v_or3_b32 v249, v249, v147, v148
	v_or3_b32 v249, v249, v149, v150
	v_or3_b32 v249, v249, v151, v152
	v_bitop3_b32 v249, v249, s31, v153 bitop3:0xc8
	v_cmp_eq_u32_e32 vcc, 0, v249
	s_cmp_eq_u64 vcc, exec
	s_cbranch_scc0 .Lrec_own_retry
.Lrec_own_ok:
	s_barrier
	ds_read_b128 v[194:197], v180
	ds_read_b128 v[198:201], v181
	ds_read_b128 v[202:205], v182
	ds_read_b128 v[206:209], v183
	ds_read_b128 v[210:213], v184
	ds_read_b128 v[214:217], v185
	ds_read_b128 v[218:221], v186
	ds_read_b128 v[222:225], v187
	ds_read_b128 v[226:229], v188
	ds_read_b128 v[230:233], v189
	ds_read_b128 v[234:237], v190
	ds_read_b128 v[238:241], v191
	s_waitcnt lgkmcnt(11)
	v_mfma_f32_16x16x32_f16 v[158:161], v[18:21], v[194:197], v[158:161]
	v_mfma_f32_16x16x32_f16 v[154:157], v[82:85], v[194:197], v[154:157]
	global_load_dwordx2 v[174:175], v243, s[52:53] nt
	s_waitcnt lgkmcnt(10)
	v_mfma_f32_16x16x32_f16 v[158:161], v[22:25], v[198:201], v[158:161]
	v_mfma_f32_16x16x32_f16 v[154:157], v[86:89], v[198:201], v[154:157]
	global_store_dword v242, v193, s[48:49] nt
	s_waitcnt lgkmcnt(9)
	v_mfma_f32_16x16x32_f16 v[158:161], v[26:29], v[202:205], v[158:161]
	v_mfma_f32_16x16x32_f16 v[154:157], v[90:93], v[202:205], v[154:157]
	s_mov_b64 exec, s[2:3]
	s_cmp_lg_u32 s57, 0
	s_cbranch_scc1 .Lrec_poi_sc1
	buffer_store_dwordx2 v[172:173], v165, s[8:11], s46 offen
	s_branch .Lrec_poi_done

.Lrec_poi_done:
	s_mov_b64 exec, -1
	s_waitcnt lgkmcnt(8)
	v_mfma_f32_16x16x32_f16 v[158:161], v[30:33], v[206:209], v[158:161]
	v_mfma_f32_16x16x32_f16 v[154:157], v[94:97], v[206:209], v[154:157]
	s_waitcnt lgkmcnt(0)
	s_cmp_eq_u32 s59, 0
	s_cbranch_scc1 .Lrec_tail1
.Lrec_tail0:
	v_mfma_f32_16x16x32_f16 v[154:157], v[98:101], v[210:213], v[154:157]
	v_mfma_f32_16x16x32_f16 v[154:157], v[102:105], v[214:217], v[154:157]
	s_xor_b32 s42, s42, 0x8000
	s_mov_b32 m0, s42
	s_and_b32 s36, s33, 7
	s_lshl_b32 s36, s36, 18
	s_add_u32 s40, s54, s36
	s_addc_u32 s41, s55, 0
	v_mfma_f32_16x16x32_f16 v[154:157], v[106:109], v[218:221], v[154:157]
	v_mfma_f32_16x16x32_f16 v[154:157], v[110:113], v[222:225], v[154:157]
	s_add_i32 s58, s33, 1
	s_and_b32 s58, s58, 7
	s_lshl_b32 s58, s58, 18
	s_add_i32 s46, s33, 6
	s_and_b32 s46, s46, 7
	s_lshl_b32 s46, s46, 18
	v_mfma_f32_16x16x32_f16 v[154:157], v[114:117], v[226:229], v[154:157]
	v_mfma_f32_16x16x32_f16 v[154:157], v[118:121], v[230:233], v[154:157]
	s_add_u32 s48, s48, 0x80000
	s_addc_u32 s49, s49, 0
	s_add_i32 s36, s33, 2
	s_min_u32 s36, s36, 0xff
	s_lshr_b32 s37, s36, 1
	s_lshl_b32 s37, s37, 21
	v_mfma_f32_16x16x32_f16 v[154:157], v[122:125], v[234:237], v[154:157]
	v_mfma_f32_16x16x32_f16 v[154:157], v[126:129], v[238:241], v[154:157]
	s_and_b32 s36, s36, 1
	s_lshl_b32 s36, s36, 3
	s_or_b32 s37, s37, s36
	s_add_u32 s52, s50, s37
	s_addc_u32 s53, s51, 0
	v_mfma_f32_16x16x32_f16 v[158:161], v[34:37], v[210:213], v[158:161]
	v_mfma_f32_16x16x32_f16 v[158:161], v[38:41], v[214:217], v[158:161]
	v_mfma_f32_16x16x32_f16 v[158:161], v[42:45], v[218:221], v[158:161]
	v_mfma_f32_16x16x32_f16 v[158:161], v[46:49], v[222:225], v[158:161]
	s_nop 3
	ds_write_b128 v178, v[154:157]
	v_mfma_f32_16x16x32_f16 v[158:161], v[50:53], v[226:229], v[158:161]
	v_mfma_f32_16x16x32_f16 v[158:161], v[54:57], v[230:233], v[158:161]
	v_mfma_f32_16x16x32_f16 v[158:161], v[58:61], v[234:237], v[158:161]
	v_mfma_f32_16x16x32_f16 v[158:161], v[62:65], v[238:241], v[158:161]
	s_waitcnt lgkmcnt(0)
	s_barrier
	ds_read_b128 v[194:197], v179
	s_nop 4
	v_pk_add_f32 v[198:199], v[158:159], v[250:251]
	v_pk_add_f32 v[200:201], v[160:161], v[252:253]
	s_branch .Lrec_act
.Lrec_tail1:
	v_mfma_f32_16x16x32_f16 v[158:161], v[34:37], v[210:213], v[158:161]
	v_mfma_f32_16x16x32_f16 v[158:161], v[38:41], v[214:217], v[158:161]
	s_xor_b32 s42, s42, 0x8000
	s_mov_b32 m0, s42
	s_and_b32 s36, s33, 7
	s_lshl_b32 s36, s36, 18
	s_add_u32 s40, s54, s36
	s_addc_u32 s41, s55, 0
	v_mfma_f32_16x16x32_f16 v[158:161], v[42:45], v[218:221], v[158:161]
	v_mfma_f32_16x16x32_f16 v[158:161], v[46:49], v[222:225], v[158:161]
	s_add_i32 s58, s33, 1
	s_and_b32 s58, s58, 7
	s_lshl_b32 s58, s58, 18
	s_add_i32 s46, s33, 6
	s_and_b32 s46, s46, 7
	s_lshl_b32 s46, s46, 18
	v_mfma_f32_16x16x32_f16 v[158:161], v[50:53], v[226:229], v[158:161]
	v_mfma_f32_16x16x32_f16 v[158:161], v[54:57], v[230:233], v[158:161]
	s_add_u32 s48, s48, 0x80000
	s_addc_u32 s49, s49, 0
	s_add_i32 s36, s33, 2
	s_min_u32 s36, s36, 0xff
	s_lshr_b32 s37, s36, 1
	s_lshl_b32 s37, s37, 21
	v_mfma_f32_16x16x32_f16 v[158:161], v[58:61], v[234:237], v[158:161]
	v_mfma_f32_16x16x32_f16 v[158:161], v[62:65], v[238:241], v[158:161]
	s_and_b32 s36, s36, 1
	s_lshl_b32 s36, s36, 3
	s_or_b32 s37, s37, s36
	s_add_u32 s52, s50, s37
	s_addc_u32 s53, s51, 0
	v_mfma_f32_16x16x32_f16 v[154:157], v[98:101], v[210:213], v[154:157]
	v_mfma_f32_16x16x32_f16 v[154:157], v[102:105], v[214:217], v[154:157]
	v_mfma_f32_16x16x32_f16 v[154:157], v[106:109], v[218:221], v[154:157]
	v_mfma_f32_16x16x32_f16 v[154:157], v[110:113], v[222:225], v[154:157]
	s_nop 3
	ds_write_b128 v178, v[158:161]
	v_mfma_f32_16x16x32_f16 v[154:157], v[114:117], v[226:229], v[154:157]
	v_mfma_f32_16x16x32_f16 v[154:157], v[118:121], v[230:233], v[154:157]
	v_mfma_f32_16x16x32_f16 v[154:157], v[122:125], v[234:237], v[154:157]
	v_mfma_f32_16x16x32_f16 v[154:157], v[126:129], v[238:241], v[154:157]
	s_waitcnt lgkmcnt(0)
	s_barrier
	ds_read_b128 v[194:197], v179
	s_nop 4
	v_pk_add_f32 v[198:199], v[154:155], v[250:251]
	v_pk_add_f32 v[200:201], v[156:157], v[252:253]
.Lrec_act:
	s_add_i32 s33, s33, 1
	s_waitcnt lgkmcnt(0)
	v_pk_add_f32 v[198:199], v[198:199], v[194:195]
	v_pk_add_f32 v[200:201], v[200:201], v[196:197]
	v_exp_f32_e32 v200, v200
	v_exp_f32_e32 v199, v199
	v_exp_f32_e32 v198, v198
	v_exp_f32_e32 v201, v201
	v_add_f32_e32 v200, 1.0, v200
	v_add_f32_e32 v199, 1.0, v199
	v_add_f32_e32 v198, 1.0, v198
	v_add_f32_e32 v201, 1.0, v201
	v_rcp_f32_e32 v200, v200
	v_rcp_f32_e32 v199, v199
	v_rcp_f32_e32 v198, v198
	v_rcp_f32_e32 v201, v201
	v_fma_f32 v200, v200, -2.0, 1.0
	v_mul_f32_e32 v199, v199, v200
	v_fmac_f32_e32 v199, v192, v198
	v_mul_f32_e32 v202, 0x4038aa3b, v199
	v_exp_f32_e32 v202, v202
	v_mov_b32_e32 v192, v199
	v_add_f32_e32 v202, 1.0, v202
	v_rcp_f32_e32 v202, v202
	s_nop 0
	v_fma_f32 v202, v202, -2.0, 1.0
	v_fma_mixlo_f16 v154, v201, v202, 0
	v_mul_f32_e32 v193, v201, v202
	v_and_b32_e32 v154, 0xffff, v154
	v_mov_b32_e32 v155, v154
	s_nop 1
	v_permlane16_swap_b32_e32 v154, v155
	v_lshl_or_b32 v154, v155, 16, v154
	v_mov_b32_e32 v155, v154
	s_nop 1
	v_permlane32_swap_b32_e32 v154, v155
	s_mov_b64 exec, s[2:3]
	s_cmp_lg_u32 s57, 0
	s_cbranch_scc1 .Lrec_hst_sc1
	buffer_store_dwordx2 v[154:155], v165, s[8:11], s45 offen
	s_branch .Lrec_hst_done

	.amdhsa_kernel _Z8lstm_recPKDF16_S0_PKfPhPf
		.amdhsa_group_segment_fixed_size 73728
		.amdhsa_private_segment_fixed_size 0
		.amdhsa_kernarg_size 40
		.amdhsa_user_sgpr_count 2
		.amdhsa_user_sgpr_dispatch_ptr 0
		.amdhsa_user_sgpr_queue_ptr 0
		.amdhsa_user_sgpr_kernarg_segment_ptr 1
		.amdhsa_user_sgpr_dispatch_id 0
		.amdhsa_user_sgpr_kernarg_preload_length 0
		.amdhsa_user_sgpr_kernarg_preload_offset 0
		.amdhsa_user_sgpr_private_segment_size 0
		.amdhsa_uses_dynamic_stack 0
		.amdhsa_enable_private_segment 0
		.amdhsa_system_sgpr_workgroup_id_x 1
		.amdhsa_system_sgpr_workgroup_id_y 0
		.amdhsa_system_sgpr_workgroup_id_z 0
		.amdhsa_system_sgpr_workgroup_info 0
		.amdhsa_system_vgpr_workitem_id 0
		.amdhsa_next_free_vgpr 256
		.amdhsa_next_free_sgpr 96
		.amdhsa_accum_offset 256
		.amdhsa_reserve_vcc 1
		.amdhsa_float_round_mode_32 0
		.amdhsa_float_round_mode_16_64 0
		.amdhsa_float_denorm_mode_32 3
		.amdhsa_float_denorm_mode_16_64 3
		.amdhsa_dx10_clamp 1
		.amdhsa_ieee_mode 1
		.amdhsa_fp16_overflow 0
		.amdhsa_tg_split 0
		.amdhsa_exception_fp_ieee_invalid_op 0
		.amdhsa_exception_fp_denorm_src 0
		.amdhsa_exception_fp_ieee_div_zero 0
		.amdhsa_exception_fp_ieee_overflow 0
		.amdhsa_exception_fp_ieee_underflow 0
		.amdhsa_exception_fp_ieee_inexact 0
		.amdhsa_exception_int_div_zero 0
	.end_amdhsa_kernel

amdhsa.kernels:
  - .agpr_count:     0
    .args:
      - .actual_access:  read_only
        .address_space:  global
        .offset:         0
        .size:           8
        .value_kind:     global_buffer
      - .actual_access:  write_only
        .address_space:  global
        .offset:         8
        .size:           8
        .value_kind:     global_buffer
      - .actual_access:  read_only
        .address_space:  global
        .offset:         16
        .size:           8
        .value_kind:     global_buffer
      - .actual_access:  read_only
        .address_space:  global
        .offset:         24
        .size:           8
        .value_kind:     global_buffer
      - .actual_access:  read_only
        .address_space:  global
        .offset:         32
        .size:           8
        .value_kind:     global_buffer
      - .actual_access:  read_only
        .address_space:  global
        .offset:         40
        .size:           8
        .value_kind:     global_buffer
      - .actual_access:  read_only
        .address_space:  global
        .offset:         48
        .size:           8
        .value_kind:     global_buffer
      - .actual_access:  read_only
        .address_space:  global
        .offset:         56
        .size:           8
        .value_kind:     global_buffer
      - .actual_access:  read_only
        .address_space:  global
        .offset:         64
        .size:           8
        .value_kind:     global_buffer
      - .actual_access:  read_only
        .address_space:  global
        .offset:         72
        .size:           8
        .value_kind:     global_buffer
      - .actual_access:  write_only
        .address_space:  global
        .offset:         80
        .size:           8
        .value_kind:     global_buffer
      - .actual_access:  write_only
        .address_space:  global
        .offset:         88
        .size:           8
        .value_kind:     global_buffer
      - .actual_access:  write_only
        .address_space:  global
        .offset:         96
        .size:           8
        .value_kind:     global_buffer
      - .actual_access:  write_only
        .address_space:  global
        .offset:         104
        .size:           8
        .value_kind:     global_buffer
    .group_segment_fixed_size: 0
    .kernarg_segment_align: 8
    .kernarg_segment_size: 112
    .language:       OpenCL C
    .language_version:
      - 2
      - 0
    .max_flat_workgroup_size: 256
    .name:           _Z4prepPKfPDF16_S0_S0_S0_S0_S0_S0_S0_S0_S1_S1_PfPh
    .private_segment_fixed_size: 0
    .sgpr_count:     32
    .sgpr_spill_count: 0
    .symbol:         _Z4prepPKfPDF16_S0_S0_S0_S0_S0_S0_S0_S0_S1_S1_PfPh.kd
    .uniform_work_group_size: 1
    .uses_dynamic_stack: false
    .vgpr_count:     16
    .vgpr_spill_count: 0
    .wavefront_size: 64
  - .agpr_count:     0
    .args:
      - .address_space:  global
        .offset:         0
        .size:           8
        .value_kind:     global_buffer
      - .address_space:  global
        .offset:         8
        .size:           8
        .value_kind:     global_buffer
      - .actual_access:  write_only
        .address_space:  global
        .offset:         16
        .size:           8
        .value_kind:     global_buffer
    .group_segment_fixed_size: 0
    .kernarg_segment_align: 8
    .kernarg_segment_size: 24
    .language:       OpenCL C
    .language_version:
      - 2
      - 0
    .max_flat_workgroup_size: 512
    .name:           _Z7gemm_zxPKDF16_S0_PDF16_
    .private_segment_fixed_size: 0
    .sgpr_count:     48
    .sgpr_spill_count: 0
    .symbol:         _Z7gemm_zxPKDF16_S0_PDF16_.kd
    .uniform_work_group_size: 1
    .uses_dynamic_stack: false
    .vgpr_count:     256
    .vgpr_spill_count: 0
    .wavefront_size: 64
  - .agpr_count:     0
    .args:
      - .actual_access:  read_only
        .address_space:  global
        .offset:         0
        .size:           8
        .value_kind:     global_buffer
      - .actual_access:  read_only
        .address_space:  global
        .offset:         8
        .size:           8
        .value_kind:     global_buffer
      - .actual_access:  read_only
        .address_space:  global
        .offset:         16
        .size:           8
        .value_kind:     global_buffer
      - .address_space:  global
        .offset:         24
        .size:           8
        .value_kind:     global_buffer
      - .actual_access:  write_only
        .address_space:  global
        .offset:         32
        .size:           8
        .value_kind:     global_buffer
    .group_segment_fixed_size: 73728
    .kernarg_segment_align: 8
    .kernarg_segment_size: 40
    .language:       OpenCL C
    .language_version:
      - 2
      - 0
    .max_flat_workgroup_size: 512
    .name:           _Z8lstm_recPKDF16_S0_PKfPhPf
    .private_segment_fixed_size: 0
    .sgpr_count:     66
    .sgpr_spill_count: 0
    .symbol:         _Z8lstm_recPKDF16_S0_PKfPhPf.kd
    .uniform_work_group_size: 1
    .uses_dynamic_stack: false
    .vgpr_count:     256
    .vgpr_spill_count: 0
    .wavefront_size: 64
